# speedup vs baseline: 1.0181x; 1.0181x over previous
.Lc_wait0:
	ds_read_b32 v37, v36
	ds_read_b32 v38, v36 offset:64
	s_waitcnt lgkmcnt(0)
	v_readfirstlane_b32 s4, v37
	v_readfirstlane_b32 s5, v38
	s_and_b32 s4, s4, s5
	s_cbranch_scc1 .Lc_go
	s_sleep 1
	s_add_i32 s73, s73, 1
	s_cmp_lt_u32 s73, 0x4000
	s_cbranch_scc1 .Lc_wait0
	s_nop 0
